# P10 in-loop workgroup barriers now guarded by a workgroup-uniform token-count check (no behaviour change on 256 CUs)
# speedup vs baseline: 1.0229x; 1.0033x over previous
; #define EXP_ROW(src, l) (*(const u32x4*)(UV + ((unsigned)__builtin_amdgcn_readlane((src), (l)) * 1024u + lo16)))
; #define EXP_XROW(tt) do { const char* g_ = (const char*)(xin + (size_t)(tt) * 1024) + lane * 16; LAS unsigned char* l_ = xslot + ((tt) & 1) * 2048; \
;         __builtin_amdgcn_global_load_lds((const unsigned*)g_, (LAS unsigned*)l_, 16, 0, 2); __builtin_amdgcn_global_load_lds((const unsigned*)(g_ + 1024), (LAS unsigned*)(l_ + 1024), 16, 0, 2); } while (0)
; __device__ __forceinline__ void expert_tokens(const unsigned char* __restrict__ UV, const float* __restrict__ US, const float* __restrict__ VS, ...
;     if (t0 >= t1) return;
;     const unsigned lo16 = (unsigned)lane * 16u;
;     const int el = ((lane >> 5) & 1) * 8 + ((lane >> 4) & 1) * 4 + ((lane >> 1) & 1) * 2 + (lane & 1);
;     const unsigned cw0 = (unsigned)IDX[(size_t)t0 * 128 + lane], cw1 = (unsigned)IDX[(size_t)t0 * 128 + 64 + lane];
;     int ci0 = (int)cw0 & rmask, ci1 = (int)cw1 & rmask;
;     float cg0 = __uint_as_float(cw0 & 0xFFFF0000u), cg1 = __uint_as_float(cw1 & 0xFFFF0000u);
;     float csu0 = US[ci0], csu1 = US[ci1], csv0 = VS[ci0], csv1 = VS[ci1];
;     ...
;     EXP_XROW(t0);
;     u32x4 A[EB], B[EB];
; #pragma unroll
;     for (int e = 0; e < EB; ++e) A[e] = EXP_ROW(ci0, e);
; #pragma unroll
;     for (int e = 0; e < EB; ++e) B[e] = EXP_ROW(ci0, EB + e);
.LBB0_1011:
	s_or_b64 exec, exec, s[12:13]
	s_waitcnt lgkmcnt(0)
	s_mul_i32 s8, s24, s96
	s_add_i32 s0, s8, s24
	s_min_i32 s17, s0, 0x8000
	s_sub_i32 s77, s96, s95
	s_add_i32 s77, s77, 8
	s_mul_i32 s77, s77, s24
	s_cmp_le_i32 s77, 0x8000
	s_cselect_b32 s77, 1, 0
	s_cmp_ge_i32 s8, s17
	s_waitcnt vmcnt(0)
	s_barrier
	s_cbranch_scc1 .LBB0_1025
	s_add_u32 s0, s6, 0xf800000
	s_addc_u32 s1, s7, 0
	s_add_u32 s10, s6, 0x1200000
	s_addc_u32 s11, s7, 0
	s_add_u32 s12, s6, 0x1100000
	s_addc_u32 s13, s7, 0
	s_add_u32 s14, s6, 0x1140000
	s_addc_u32 s15, s7, 0
	s_lshl_b32 s2, s95, 12
	s_add_i32 s26, s2, 0
	s_add_u32 s2, s6, 0x1b800000
	s_addc_u32 s3, s7, 0
	s_ashr_i32 s9, s8, 31
	s_lshl_b64 s[6:7], s[8:9], 9
	v_and_b32_e32 v74, 63, v0
	s_add_u32 s6, s0, s6
	s_addc_u32 s7, s1, s7
	v_lshlrev_b32_e32 v192, 2, v74
	global_load_dword v229, v192, s[6:7]
	global_load_dword v230, v192, s[6:7] offset:256
	s_lshl_b64 s[18:19], s[8:9], 11
	s_add_u32 s18, s2, s18
	s_addc_u32 s19, s3, s19
	s_lshl_b32 s9, s8, 11
	v_mov_b32_e32 v1, 0
	s_and_b32 s9, s9, 0x800
	v_lshlrev_b32_e32 v194, 4, v74
	v_mov_b32_e32 v195, v1
	s_add_i32 s9, s26, s9
	s_mov_b64 s[6:7], 0x400
	v_lshl_add_u64 v[2:3], s[18:19], 0, v[194:195]
	s_add_i32 m0, s9, 0x4000
	v_lshl_add_u64 v[2:3], v[2:3], 0, s[6:7]
	global_load_lds_dwordx4 v194, s[18:19] nt
	s_add_i32 m0, s9, 0x4400
	v_mov_b32_e32 v193, v1
	global_load_lds_dwordx4 v[2:3], off nt
	v_and_b32_e32 v77, 2, v0
	v_lshl_add_u64 v[196:197], s[0:1], 0, v[192:193]
	v_lshl_add_u64 v[198:199], s[2:3], 0, v[194:195]
	v_cmp_eq_u32_e64 s[0:1], 0, v77
	v_lshl_add_u64 v[200:201], s[4:5], 0, v[194:195]
	v_lshl_add_u32 v195, v74, 3, s26
	v_mov_b32_e32 v226, 0x358637bd
	v_mov_b32_e32 v227, 0xbf3a00e3
	s_waitcnt vmcnt(0)
	v_alignbit_b32 v229, v229, v229, 16
	v_alignbit_b32 v230, v230, v230, 16
	s_nop 1
	s_mov_b32 s58, 0x99999999
	s_mov_b32 s59, 0x99999999
	v_min_u32_dpp v202, v229, v229 quad_perm:[1,0,3,2] row_mask:0xf bank_mask:0xf
	v_max_u32_dpp v203, v229, v229 quad_perm:[1,0,3,2] row_mask:0xf bank_mask:0xf
	v_min_u32_dpp v204, v230, v230 quad_perm:[1,0,3,2] row_mask:0xf bank_mask:0xf
	v_max_u32_dpp v205, v230, v230 quad_perm:[1,0,3,2] row_mask:0xf bank_mask:0xf
	v_cndmask_b32_e64 v229, v203, v202, s[58:59]
	v_cndmask_b32_e64 v230, v205, v204, s[58:59]
	s_mov_b32 s58, 0xcc33cc33
	s_mov_b32 s59, 0xcc33cc33
	v_min_u32_dpp v202, v229, v229 quad_perm:[2,3,0,1] row_mask:0xf bank_mask:0xf
	v_max_u32_dpp v203, v229, v229 quad_perm:[2,3,0,1] row_mask:0xf bank_mask:0xf
	v_min_u32_dpp v204, v230, v230 quad_perm:[2,3,0,1] row_mask:0xf bank_mask:0xf
	v_max_u32_dpp v205, v230, v230 quad_perm:[2,3,0,1] row_mask:0xf bank_mask:0xf
	v_cndmask_b32_e64 v229, v203, v202, s[58:59]
	v_cndmask_b32_e64 v230, v205, v204, s[58:59]
	s_mov_b32 s58, 0xaa55aa55
	s_mov_b32 s59, 0xaa55aa55
	v_min_u32_dpp v202, v229, v229 quad_perm:[1,0,3,2] row_mask:0xf bank_mask:0xf
	v_max_u32_dpp v203, v229, v229 quad_perm:[1,0,3,2] row_mask:0xf bank_mask:0xf
	v_min_u32_dpp v204, v230, v230 quad_perm:[1,0,3,2] row_mask:0xf bank_mask:0xf
	v_max_u32_dpp v205, v230, v230 quad_perm:[1,0,3,2] row_mask:0xf bank_mask:0xf
	v_cndmask_b32_e64 v229, v203, v202, s[58:59]
	v_cndmask_b32_e64 v230, v205, v204, s[58:59]
	s_mov_b32 s58, 0xf00ff00f
	s_mov_b32 s59, 0xf00ff00f
	v_min_u32_dpp v202, v229, v229 row_ror:8 row_mask:0xf bank_mask:0xf
	v_max_u32_dpp v203, v229, v229 row_ror:8 row_mask:0xf bank_mask:0xf
	v_min_u32_dpp v204, v230, v230 row_ror:8 row_mask:0xf bank_mask:0xf
	v_max_u32_dpp v205, v230, v230 row_ror:8 row_mask:0xf bank_mask:0xf
	v_cndmask_b32_e64 v229, v203, v202, s[58:59]
	v_cndmask_b32_e64 v230, v205, v204, s[58:59]
	s_mov_b32 s58, 0xc3c3c3c3
	s_mov_b32 s59, 0xc3c3c3c3
	v_min_u32_dpp v202, v229, v229 quad_perm:[2,3,0,1] row_mask:0xf bank_mask:0xf
	v_max_u32_dpp v203, v229, v229 quad_perm:[2,3,0,1] row_mask:0xf bank_mask:0xf
	v_min_u32_dpp v204, v230, v230 quad_perm:[2,3,0,1] row_mask:0xf bank_mask:0xf
	v_max_u32_dpp v205, v230, v230 quad_perm:[2,3,0,1] row_mask:0xf bank_mask:0xf
	v_cndmask_b32_e64 v229, v203, v202, s[58:59]
	v_cndmask_b32_e64 v230, v205, v204, s[58:59]
	s_mov_b32 s58, 0xa5a5a5a5
	s_mov_b32 s59, 0xa5a5a5a5
	v_min_u32_dpp v202, v229, v229 quad_perm:[1,0,3,2] row_mask:0xf bank_mask:0xf
	v_max_u32_dpp v203, v229, v229 quad_perm:[1,0,3,2] row_mask:0xf bank_mask:0xf
	v_min_u32_dpp v204, v230, v230 quad_perm:[1,0,3,2] row_mask:0xf bank_mask:0xf
	v_max_u32_dpp v205, v230, v230 quad_perm:[1,0,3,2] row_mask:0xf bank_mask:0xf
	v_cndmask_b32_e64 v229, v203, v202, s[58:59]
	v_cndmask_b32_e64 v230, v205, v204, s[58:59]
	s_mov_b32 s58, 0xf0f00f0f
	s_mov_b32 s59, 0xf0f00f0f
	v_mov_b32_dpp v202, v229 row_half_mirror row_mask:0xf bank_mask:0xf
	v_mov_b32_dpp v204, v230 row_half_mirror row_mask:0xf bank_mask:0xf
	s_nop 0
	v_max_u32_dpp v203, v202, v229 quad_perm:[3,2,1,0] row_mask:0xf bank_mask:0xf
	v_max_u32_dpp v205, v204, v230 quad_perm:[3,2,1,0] row_mask:0xf bank_mask:0xf
	v_min_u32_dpp v202, v202, v229 quad_perm:[3,2,1,0] row_mask:0xf bank_mask:0xf
	v_min_u32_dpp v204, v204, v230 quad_perm:[3,2,1,0] row_mask:0xf bank_mask:0xf
	v_cndmask_b32_e64 v229, v203, v202, s[58:59]
	v_cndmask_b32_e64 v230, v205, v204, s[58:59]
	s_mov_b32 s58, 0xff0000ff
	s_mov_b32 s59, 0xff0000ff
	v_min_u32_dpp v202, v229, v229 row_ror:8 row_mask:0xf bank_mask:0xf
	v_max_u32_dpp v203, v229, v229 row_ror:8 row_mask:0xf bank_mask:0xf
	v_min_u32_dpp v204, v230, v230 row_ror:8 row_mask:0xf bank_mask:0xf
	v_max_u32_dpp v205, v230, v230 row_ror:8 row_mask:0xf bank_mask:0xf
	v_cndmask_b32_e64 v229, v203, v202, s[58:59]
	v_cndmask_b32_e64 v230, v205, v204, s[58:59]
	s_mov_b32 s58, 0xcccc3333
	s_mov_b32 s59, 0xcccc3333
; __device__ __forceinline__ void expert_tokens(const unsigned char* __restrict__ UV, const float* __restrict__ US, const float* __restrict__ VS, ...
;     ...
;     const unsigned cw0 = (unsigned)IDX[(size_t)t0 * 128 + lane], cw1 = (unsigned)IDX[(size_t)t0 * 128 + 64 + lane];
;     int ci0 = (int)cw0 & rmask, ci1 = (int)cw1 & rmask;
	v_min_u32_dpp v202, v229, v229 quad_perm:[2,3,0,1] row_mask:0xf bank_mask:0xf
	v_max_u32_dpp v203, v229, v229 quad_perm:[2,3,0,1] row_mask:0xf bank_mask:0xf
	v_min_u32_dpp v204, v230, v230 quad_perm:[2,3,0,1] row_mask:0xf bank_mask:0xf
	v_max_u32_dpp v205, v230, v230 quad_perm:[2,3,0,1] row_mask:0xf bank_mask:0xf
	v_cndmask_b32_e64 v229, v203, v202, s[58:59]
	v_cndmask_b32_e64 v230, v205, v204, s[58:59]
	s_mov_b32 s58, 0xaaaa5555
	s_mov_b32 s59, 0xaaaa5555
	v_min_u32_dpp v202, v229, v229 quad_perm:[1,0,3,2] row_mask:0xf bank_mask:0xf
	v_max_u32_dpp v203, v229, v229 quad_perm:[1,0,3,2] row_mask:0xf bank_mask:0xf
	v_min_u32_dpp v204, v230, v230 quad_perm:[1,0,3,2] row_mask:0xf bank_mask:0xf
	v_max_u32_dpp v205, v230, v230 quad_perm:[1,0,3,2] row_mask:0xf bank_mask:0xf
	v_cndmask_b32_e64 v229, v203, v202, s[58:59]
	v_cndmask_b32_e64 v230, v205, v204, s[58:59]
	s_nop 1
	v_permlane16_swap_b32_e32 v229, v230
	s_mov_b32 s58, -1
	s_mov_b32 s59, 0
	v_min_u32_e32 v202, v229, v230
	v_max_u32_e32 v203, v229, v230
	v_cndmask_b32_e64 v229, v203, v202, s[58:59]
	v_cndmask_b32_e64 v230, v202, v203, s[58:59]
	s_mov_b32 s58, 0xf0f0f0f
	s_mov_b32 s59, 0xf0f0f0f0
	v_mov_b32_dpp v202, v229 row_half_mirror row_mask:0xf bank_mask:0xf
	v_mov_b32_dpp v204, v230 row_half_mirror row_mask:0xf bank_mask:0xf
	s_nop 0
	v_max_u32_dpp v203, v202, v229 quad_perm:[3,2,1,0] row_mask:0xf bank_mask:0xf
	v_max_u32_dpp v205, v204, v230 quad_perm:[3,2,1,0] row_mask:0xf bank_mask:0xf
	v_min_u32_dpp v202, v202, v229 quad_perm:[3,2,1,0] row_mask:0xf bank_mask:0xf
	v_min_u32_dpp v204, v204, v230 quad_perm:[3,2,1,0] row_mask:0xf bank_mask:0xf
	v_cndmask_b32_e64 v229, v203, v202, s[58:59]
	v_cndmask_b32_e64 v230, v205, v204, s[58:59]
	s_mov_b32 s58, 0xff00ff
	s_mov_b32 s59, 0xff00ff00
	v_min_u32_dpp v202, v229, v229 row_ror:8 row_mask:0xf bank_mask:0xf
	v_max_u32_dpp v203, v229, v229 row_ror:8 row_mask:0xf bank_mask:0xf
	v_min_u32_dpp v204, v230, v230 row_ror:8 row_mask:0xf bank_mask:0xf
	v_max_u32_dpp v205, v230, v230 row_ror:8 row_mask:0xf bank_mask:0xf
	v_cndmask_b32_e64 v229, v203, v202, s[58:59]
	v_cndmask_b32_e64 v230, v205, v204, s[58:59]
	s_mov_b32 s58, 0x33333333
	s_mov_b32 s59, 0xcccccccc
	v_min_u32_dpp v202, v229, v229 quad_perm:[2,3,0,1] row_mask:0xf bank_mask:0xf
	v_max_u32_dpp v203, v229, v229 quad_perm:[2,3,0,1] row_mask:0xf bank_mask:0xf
	v_min_u32_dpp v204, v230, v230 quad_perm:[2,3,0,1] row_mask:0xf bank_mask:0xf
	v_max_u32_dpp v205, v230, v230 quad_perm:[2,3,0,1] row_mask:0xf bank_mask:0xf
	v_cndmask_b32_e64 v229, v203, v202, s[58:59]
	v_cndmask_b32_e64 v230, v205, v204, s[58:59]
	s_mov_b32 s58, 0x55555555
	s_mov_b32 s59, 0xaaaaaaaa
	v_min_u32_dpp v202, v229, v229 quad_perm:[1,0,3,2] row_mask:0xf bank_mask:0xf
	v_max_u32_dpp v203, v229, v229 quad_perm:[1,0,3,2] row_mask:0xf bank_mask:0xf
	v_min_u32_dpp v204, v230, v230 quad_perm:[1,0,3,2] row_mask:0xf bank_mask:0xf
	v_max_u32_dpp v205, v230, v230 quad_perm:[1,0,3,2] row_mask:0xf bank_mask:0xf
	v_cndmask_b32_e64 v229, v203, v202, s[58:59]
	v_cndmask_b32_e64 v230, v205, v204, s[58:59]
	s_nop 1
	v_permlane32_swap_b32_e32 v229, v230
	s_mov_b32 s58, 0xffff
	s_mov_b32 s59, 0xffff
	v_min_u32_e32 v202, v229, v230
	v_max_u32_e32 v203, v229, v230
	v_cndmask_b32_e64 v229, v203, v202, s[58:59]
	v_cndmask_b32_e64 v230, v202, v203, s[58:59]
	s_nop 1
	v_permlane32_swap_b32_e32 v229, v230
	s_mov_b32 s58, 0xffff
	s_mov_b32 s59, 0xffff
	v_min_u32_e32 v202, v229, v230
	v_max_u32_e32 v203, v229, v230
	v_cndmask_b32_e64 v229, v203, v202, s[58:59]
	v_cndmask_b32_e64 v230, v202, v203, s[58:59]
	s_mov_b32 s58, 0xf0f00f0f
	s_mov_b32 s59, 0xf0f00f0f
	v_mov_b32_dpp v202, v229 row_half_mirror row_mask:0xf bank_mask:0xf
	v_mov_b32_dpp v204, v230 row_half_mirror row_mask:0xf bank_mask:0xf
	s_nop 0
	v_max_u32_dpp v203, v202, v229 quad_perm:[3,2,1,0] row_mask:0xf bank_mask:0xf
	v_max_u32_dpp v205, v204, v230 quad_perm:[3,2,1,0] row_mask:0xf bank_mask:0xf
	v_min_u32_dpp v202, v202, v229 quad_perm:[3,2,1,0] row_mask:0xf bank_mask:0xf
	v_min_u32_dpp v204, v204, v230 quad_perm:[3,2,1,0] row_mask:0xf bank_mask:0xf
	v_cndmask_b32_e64 v229, v203, v202, s[58:59]
	v_cndmask_b32_e64 v230, v205, v204, s[58:59]
	s_mov_b32 s58, 0xff0000ff
	s_mov_b32 s59, 0xff0000ff
	v_min_u32_dpp v202, v229, v229 row_ror:8 row_mask:0xf bank_mask:0xf
	v_max_u32_dpp v203, v229, v229 row_ror:8 row_mask:0xf bank_mask:0xf
	v_min_u32_dpp v204, v230, v230 row_ror:8 row_mask:0xf bank_mask:0xf
	v_max_u32_dpp v205, v230, v230 row_ror:8 row_mask:0xf bank_mask:0xf
	v_cndmask_b32_e64 v229, v203, v202, s[58:59]
	v_cndmask_b32_e64 v230, v205, v204, s[58:59]
	s_mov_b32 s58, 0xcccc3333
	s_mov_b32 s59, 0xcccc3333
	v_min_u32_dpp v202, v229, v229 quad_perm:[2,3,0,1] row_mask:0xf bank_mask:0xf
	v_max_u32_dpp v203, v229, v229 quad_perm:[2,3,0,1] row_mask:0xf bank_mask:0xf
	v_min_u32_dpp v204, v230, v230 quad_perm:[2,3,0,1] row_mask:0xf bank_mask:0xf
	v_max_u32_dpp v205, v230, v230 quad_perm:[2,3,0,1] row_mask:0xf bank_mask:0xf
	v_cndmask_b32_e64 v229, v203, v202, s[58:59]
	v_cndmask_b32_e64 v230, v205, v204, s[58:59]
	s_mov_b32 s58, 0xaaaa5555
	s_mov_b32 s59, 0xaaaa5555
	v_min_u32_dpp v202, v229, v229 quad_perm:[1,0,3,2] row_mask:0xf bank_mask:0xf
	v_max_u32_dpp v203, v229, v229 quad_perm:[1,0,3,2] row_mask:0xf bank_mask:0xf
	v_min_u32_dpp v204, v230, v230 quad_perm:[1,0,3,2] row_mask:0xf bank_mask:0xf
	v_max_u32_dpp v205, v230, v230 quad_perm:[1,0,3,2] row_mask:0xf bank_mask:0xf
	v_cndmask_b32_e64 v229, v203, v202, s[58:59]
	v_cndmask_b32_e64 v230, v205, v204, s[58:59]
	s_nop 1
	v_permlane16_swap_b32_e32 v229, v230
	v_min_u32_e32 v202, v229, v230
	v_max_u32_e32 v230, v229, v230
	v_mov_b32_e32 v229, v202
; #define EXP_ROW(src, l) (*(const u32x4*)(UV + ((unsigned)__builtin_amdgcn_readlane((src), (l)) * 1024u + lo16)))
; #define EXP_XROW(tt) do { const char* g_ = (const char*)(xin + (size_t)(tt) * 1024) + lane * 16; LAS unsigned char* l_ = xslot + ((tt) & 1) * 2048; \
;         __builtin_amdgcn_global_load_lds((const unsigned*)g_, (LAS unsigned*)l_, 16, 0, 2); __builtin_amdgcn_global_load_lds((const unsigned*)(g_ + 1024), (LAS unsigned*)(l_ + 1024), 16, 0, 2); } while (0)
; __device__ __forceinline__ void expert_tokens(const unsigned char* __restrict__ UV, const float* __restrict__ US, const float* __restrict__ VS, ...
;     ...
;     int ci0 = (int)cw0 & rmask, ci1 = (int)cw1 & rmask;
;     float cg0 = __uint_as_float(cw0 & 0xFFFF0000u), cg1 = __uint_as_float(cw1 & 0xFFFF0000u);
;     float csu0 = US[ci0], csu1 = US[ci1], csv0 = VS[ci0], csv1 = VS[ci1];
;     ...
;     EXP_XROW(t0);
;     u32x4 A[EB], B[EB];
; #pragma unroll
;     for (int e = 0; e < EB; ++e) A[e] = EXP_ROW(ci0, e);
; #pragma unroll
;     for (int e = 0; e < EB; ++e) B[e] = EXP_ROW(ci0, EB + e);
	s_nop 1
	v_permlane32_swap_b32_e32 v229, v230
	v_min_u32_e32 v202, v229, v230
	v_max_u32_e32 v230, v229, v230
	v_mov_b32_e32 v229, v202
	s_nop 1
	v_permlane16_swap_b32_e32 v229, v230
	v_min_u32_e32 v202, v229, v230
	v_max_u32_e32 v230, v229, v230
	v_mov_b32_e32 v229, v202
	s_mov_b32 s58, 0xf0f0f0f
	s_mov_b32 s59, 0xf0f0f0f
	v_mov_b32_dpp v202, v229 row_half_mirror row_mask:0xf bank_mask:0xf
	v_mov_b32_dpp v204, v230 row_half_mirror row_mask:0xf bank_mask:0xf
	s_nop 0
	v_max_u32_dpp v203, v202, v229 quad_perm:[3,2,1,0] row_mask:0xf bank_mask:0xf
	v_max_u32_dpp v205, v204, v230 quad_perm:[3,2,1,0] row_mask:0xf bank_mask:0xf
	v_min_u32_dpp v202, v202, v229 quad_perm:[3,2,1,0] row_mask:0xf bank_mask:0xf
	v_min_u32_dpp v204, v204, v230 quad_perm:[3,2,1,0] row_mask:0xf bank_mask:0xf
	v_cndmask_b32_e64 v229, v203, v202, s[58:59]
	v_cndmask_b32_e64 v230, v205, v204, s[58:59]
	s_mov_b32 s58, 0xff00ff
	s_mov_b32 s59, 0xff00ff
	v_min_u32_dpp v202, v229, v229 row_ror:8 row_mask:0xf bank_mask:0xf
	v_max_u32_dpp v203, v229, v229 row_ror:8 row_mask:0xf bank_mask:0xf
	v_min_u32_dpp v204, v230, v230 row_ror:8 row_mask:0xf bank_mask:0xf
	v_max_u32_dpp v205, v230, v230 row_ror:8 row_mask:0xf bank_mask:0xf
	v_cndmask_b32_e64 v229, v203, v202, s[58:59]
	v_cndmask_b32_e64 v230, v205, v204, s[58:59]
	s_mov_b32 s58, 0x33333333
	s_mov_b32 s59, 0x33333333
	v_min_u32_dpp v202, v229, v229 quad_perm:[2,3,0,1] row_mask:0xf bank_mask:0xf
	v_max_u32_dpp v203, v229, v229 quad_perm:[2,3,0,1] row_mask:0xf bank_mask:0xf
	v_min_u32_dpp v204, v230, v230 quad_perm:[2,3,0,1] row_mask:0xf bank_mask:0xf
	v_max_u32_dpp v205, v230, v230 quad_perm:[2,3,0,1] row_mask:0xf bank_mask:0xf
	v_cndmask_b32_e64 v229, v203, v202, s[58:59]
	v_cndmask_b32_e64 v230, v205, v204, s[58:59]
	s_mov_b32 s58, 0x55555555
	s_mov_b32 s59, 0x55555555
	v_min_u32_dpp v202, v229, v229 quad_perm:[1,0,3,2] row_mask:0xf bank_mask:0xf
	v_max_u32_dpp v203, v229, v229 quad_perm:[1,0,3,2] row_mask:0xf bank_mask:0xf
	v_min_u32_dpp v204, v230, v230 quad_perm:[1,0,3,2] row_mask:0xf bank_mask:0xf
	v_max_u32_dpp v205, v230, v230 quad_perm:[1,0,3,2] row_mask:0xf bank_mask:0xf
	v_cndmask_b32_e64 v229, v203, v202, s[58:59]
	v_cndmask_b32_e64 v230, v205, v204, s[58:59]
	s_nop 1
	v_permlane16_swap_b32_e32 v229, v230
	s_nop 1
	v_permlane32_swap_b32_e32 v229, v230
	v_alignbit_b32 v229, v229, v229, 16
	v_alignbit_b32 v230, v230, v230, 16
	v_and_b32_e32 v231, 0x3fff, v229
	v_and_b32_e32 v232, 0x3fff, v230
	v_readlane_b32 s40, v231, 22
	v_readlane_b32 s41, v231, 23
	v_readlane_b32 s49, v231, 31
	v_lshlrev_b32_e32 v2, 2, v231
	v_lshlrev_b32_e32 v3, 2, v232
	v_readlane_b32 s33, v231, 15
	v_readlane_b32 s34, v231, 16
	v_readlane_b32 s35, v231, 17
	v_readlane_b32 s36, v231, 18
	v_readlane_b32 s37, v231, 19
	v_readlane_b32 s38, v231, 20
	v_readlane_b32 s39, v231, 21
	v_readlane_b32 s42, v231, 24
	v_readlane_b32 s43, v231, 25
	v_readlane_b32 s44, v231, 26
	v_readlane_b32 s45, v231, 27
	v_readlane_b32 s46, v231, 28
	v_readlane_b32 s47, v231, 29
	v_readlane_b32 s48, v231, 30
	v_lshl_or_b32 v42, s49, 10, v194
	v_lshl_or_b32 v50, s41, 10, v194
	v_lshl_or_b32 v51, s40, 10, v194
	v_readlane_b32 s30, v231, 13
	v_readlane_b32 s31, v231, 14
	global_load_dword v233, v2, s[12:13]
	global_load_dword v234, v3, s[12:13]
	global_load_dword v236, v3, s[14:15]
	global_load_dword v235, v2, s[14:15]
	v_lshl_or_b32 v43, s48, 10, v194
	v_lshl_or_b32 v44, s47, 10, v194
	v_lshl_or_b32 v45, s46, 10, v194
	v_lshl_or_b32 v46, s45, 10, v194
	v_lshl_or_b32 v47, s44, 10, v194
	v_lshl_or_b32 v48, s43, 10, v194
	v_lshl_or_b32 v49, s42, 10, v194
	global_load_dwordx4 v[2:5], v42, s[10:11]
	global_load_dwordx4 v[10:13], v43, s[10:11]
	global_load_dwordx4 v[6:9], v44, s[10:11]
	global_load_dwordx4 v[18:21], v45, s[10:11]
	global_load_dwordx4 v[14:17], v46, s[10:11]
	global_load_dwordx4 v[26:29], v47, s[10:11]
	global_load_dwordx4 v[22:25], v48, s[10:11]
	global_load_dwordx4 v[34:37], v49, s[10:11]
	global_load_dwordx4 v[30:33], v50, s[10:11]
	global_load_dwordx4 v[38:41], v51, s[10:11]
	v_lshl_or_b32 v50, s39, 10, v194
	v_lshl_or_b32 v51, s38, 10, v194
	v_lshl_or_b32 v58, s37, 10, v194
	v_lshl_or_b32 v59, s36, 10, v194
	v_lshl_or_b32 v66, s35, 10, v194
	v_lshl_or_b32 v67, s34, 10, v194
	v_lshl_or_b32 v75, s33, 10, v194
	v_readlane_b32 s28, v231, 11
	v_readlane_b32 s29, v231, 12
	global_load_dwordx4 v[42:45], v50, s[10:11]
	global_load_dwordx4 v[46:49], v51, s[10:11]
	s_nop 0
	global_load_dwordx4 v[50:53], v58, s[10:11]
	global_load_dwordx4 v[54:57], v59, s[10:11]
	s_nop 0
	global_load_dwordx4 v[58:61], v66, s[10:11]
	global_load_dwordx4 v[62:65], v67, s[10:11]
	v_lshl_or_b32 v76, s31, 10, v194
	global_load_dwordx4 v[66:69], v75, s[10:11]
	global_load_dwordx4 v[70:73], v76, s[10:11]
	v_lshl_or_b32 v75, s30, 10, v194
	v_readlane_b32 s25, v231, 9
	v_readlane_b32 s27, v231, 10
	v_lshl_or_b32 v76, s29, 10, v194
	global_load_dwordx4 v[112:115], v75, s[10:11]
	global_load_dwordx4 v[116:119], v76, s[10:11]
	v_lshl_or_b32 v75, s28, 10, v194
	v_readlane_b32 s23, v231, 7
	v_readlane_b32 s24, v231, 8
	v_lshl_or_b32 v76, s27, 10, v194
	global_load_dwordx4 v[144:147], v75, s[10:11]
	global_load_dwordx4 v[148:151], v76, s[10:11]
	v_lshl_or_b32 v75, s25, 10, v194
	v_readlane_b32 s21, v231, 5
	v_readlane_b32 s22, v231, 6
	v_lshl_or_b32 v76, s24, 10, v194
	global_load_dwordx4 v[152:155], v75, s[10:11]
	global_load_dwordx4 v[156:159], v76, s[10:11]
	v_lshl_or_b32 v75, s23, 10, v194
	v_readlane_b32 s19, v231, 3
	v_readlane_b32 s20, v231, 4
	v_lshl_or_b32 v76, s22, 10, v194
	global_load_dwordx4 v[160:163], v75, s[10:11]
	global_load_dwordx4 v[164:167], v76, s[10:11]
	v_lshl_or_b32 v75, s21, 10, v194
	v_readlane_b32 s16, v231, 1
	v_readlane_b32 s18, v231, 2
	v_lshl_or_b32 v76, s20, 10, v194
	global_load_dwordx4 v[168:171], v75, s[10:11]
	global_load_dwordx4 v[172:175], v76, s[10:11]
	v_lshl_or_b32 v75, s19, 10, v194
	v_readlane_b32 s9, v231, 0
	v_lshl_or_b32 v76, s18, 10, v194
	global_load_dwordx4 v[176:179], v75, s[10:11]
	global_load_dwordx4 v[180:183], v76, s[10:11]
	v_lshl_or_b32 v75, s16, 10, v194
	v_lshl_or_b32 v76, s9, 10, v194
	global_load_dwordx4 v[184:187], v75, s[10:11]
	global_load_dwordx4 v[188:191], v76, s[10:11]
	v_and_b32_e32 v75, 1, v0
	v_lshrrev_b32_e32 v76, 2, v0
	v_and_b32_e32 v0, 3, v0
	v_and_or_b32 v193, v76, 12, v0
	v_cmp_eq_u32_e64 s[2:3], 0, v75
	v_mbcnt_lo_u32_b32 v0, -1, 0
	s_mov_b32 s9, 0x800000
	s_mov_b32 s16, 0x45800000
	s_mov_b32 s27, 0x42ee0000
	s_mov_b32 s28, 0x3e6d3388
	s_mov_b32 s29, 0xc040c00
	s_mov_b32 s30, 0xc050c01
	s_mov_b32 s31, 0xc060c02
	s_mov_b32 s33, 0xc070c03
	v_mbcnt_hi_u32_b32 v228, -1, v0
	s_mov_b32 s20, s8
	s_branch .LBB0_1014

; __device__ __forceinline__ void expert_tokens(const unsigned char* __restrict__ UV, const float* __restrict__ US, const float* __restrict__ VS, ...
;     ...
;     for (int t = t0; t < t1; ++t) {
;         const bool has_next = t + 1 < t1; const int tn = has_next ? t + 1 : t;
.LBB0_1014:
	s_cmp_eq_u32 s77, 0
	s_cbranch_scc1 .Lp10_nobar_t
	s_barrier
